# U3f counted-wait fix: bias load hoisted to the prologue so the MFMA chains no longer wait for the y stores to be acknowledged
# speedup vs baseline: 1.0044x; 1.0020x over previous
_Z4k_U3ILb0EtEvPKtPtPKdPKfS6_PK15HIP_vector_typeIjLj4EES6_PT0_SC_S6_Pd:
	s_cmpk_ge_u32 s2, 0x300
	s_cbranch_scc1 .LBB9_4
	s_load_dwordx2 s[4:5], s[0:1], 0x28
	s_load_dwordx4 s[20:23], s[0:1], 0x0
	s_load_dwordx2 s[24:25], s[0:1], 0x30
	v_mov_b32_e32 v3, 0
	v_lshlrev_b32_e32 v2, 4, v0
	v_or_b32_e32 v1, 0x4000, v2
	s_movk_i32 s3, 0x1000
	s_waitcnt lgkmcnt(0)
	v_lshrrev_b32_e32 v78, 6, v0
	v_lshl_add_u32 v78, s2, 2, v78
	v_and_b32_e32 v79, 31, v0
	v_lshl_or_b32 v78, v78, 5, v79
	v_and_b32_e32 v79, 32, v0
	v_lshlrev_b32_e32 v78, 7, v78
	v_lshl_add_u32 v78, v79, 1, v78
	global_load_dwordx4 v[44:47], v78, s[22:23] offset:48
	global_load_dwordx4 v[48:51], v78, s[22:23] offset:32
	global_load_dwordx4 v[52:55], v78, s[22:23] offset:16
	global_load_dwordx4 v[56:59], v78, s[22:23]
	global_load_dwordx4 v[60:63], v78, s[20:21] offset:48
	global_load_dwordx4 v[64:67], v78, s[20:21] offset:32
	global_load_dwordx4 v[68:71], v78, s[20:21] offset:16
	global_load_dwordx4 v[72:75], v78, s[20:21]
	v_and_b32_e32 v79, 31, v0
	v_lshlrev_b32_e32 v79, 3, v79
	global_load_dwordx2 a[0:1], v79, s[24:25]
	v_lshl_add_u64 v[32:33], s[4:5], 0, v[2:3]
	v_add_co_u32_e32 v24, vcc, 0x1000, v32
	global_load_dwordx4 v[4:7], v2, s[4:5]
	s_nop 0
	v_addc_co_u32_e32 v25, vcc, 0, v33, vcc
	v_add_co_u32_e32 v26, vcc, 0x2000, v32
	s_nop 1
	v_addc_co_u32_e32 v27, vcc, 0, v33, vcc
	v_add_co_u32_e32 v28, vcc, 0x3000, v32
	s_nop 1
	v_addc_co_u32_e32 v29, vcc, 0, v33, vcc
	v_add_co_u32_e32 v34, vcc, 0x5000, v32
	global_load_dwordx4 v[8:11], v[26:27], off
	global_load_dwordx4 v[12:15], v[28:29], off
	global_load_dwordx4 v[16:19], v[24:25], off
	global_load_dwordx4 v[20:23], v1, s[4:5]
	v_addc_co_u32_e32 v35, vcc, 0, v33, vcc
	v_add_co_u32_e32 v36, vcc, 0x6000, v32
	s_nop 1
	v_addc_co_u32_e32 v37, vcc, 0, v33, vcc
	global_load_dwordx4 v[24:27], v[34:35], off
	global_load_dwordx4 v[28:31], v[36:37], off
	v_add_co_u32_e32 v32, vcc, 0x7000, v32
	s_nop 1
	v_addc_co_u32_e32 v33, vcc, 0, v33, vcc
	global_load_dwordx4 v[32:35], v[32:33], off
	v_cmp_gt_u32_e32 vcc, 64, v0
	s_waitcnt vmcnt(7)
	ds_write_b128 v2, v[4:7]
	s_waitcnt vmcnt(4)
	ds_write_b128 v2, v[16:19] offset:4096
	s_waitcnt vmcnt(3)
	ds_write_b128 v2, v[20:23] offset:16384
	ds_write_b128 v2, v[8:11] offset:8192
	ds_write_b128 v2, v[12:15] offset:12288
	s_waitcnt vmcnt(2)
	ds_write_b128 v2, v[24:27] offset:20480
	s_waitcnt vmcnt(1)
	ds_write_b128 v2, v[28:31] offset:24576
	s_waitcnt vmcnt(0)
	ds_write_b128 v2, v[32:35] offset:28672
	v_lshlrev_b32_e32 v10, 2, v0
	s_and_saveexec_b64 s[6:7], vcc
	s_cbranch_execz .LBB9_2
	s_load_dwordx4 s[8:11], s[0:1], 0x10
	s_load_dwordx2 s[4:5], s[0:1], 0x20
	v_lshlrev_b32_e32 v2, 3, v0
	s_mov_b32 s12, 0
	s_brev_b32 s13, 8
	s_waitcnt lgkmcnt(0)
	global_load_dwordx2 v[6:7], v2, s[8:9]
	global_load_dwordx2 v[8:9], v2, s[8:9] offset:512
	global_load_dwordx2 v[12:13], v2, s[8:9] offset:1024
	global_load_dwordx2 v[14:15], v2, s[8:9] offset:1536
	global_load_dwordx2 v[16:17], v2, s[8:9] offset:2048
	global_load_dwordx2 v[18:19], v2, s[8:9] offset:2560
	global_load_dwordx2 v[20:21], v2, s[8:9] offset:3072
	global_load_dwordx2 v[22:23], v2, s[8:9] offset:3584
	v_lshl_add_u64 v[4:5], s[8:9], 0, v[2:3]
	v_add_co_u32_e32 v2, vcc, s3, v4
	s_mov_b32 s8, 0x88e368f1
	s_nop 0
	v_addc_co_u32_e32 v3, vcc, 0, v5, vcc
	global_load_dwordx2 v[4:5], v[2:3], off
	global_load_dwordx2 v[24:25], v[2:3], off offset:512
	global_load_dwordx2 v[26:27], v[2:3], off offset:1024
	global_load_dwordx2 v[28:29], v[2:3], off offset:1536
	global_load_dwordx2 v[30:31], v[2:3], off offset:2048
	global_load_dwordx2 v[32:33], v[2:3], off offset:2560
	global_load_dwordx2 v[34:35], v[2:3], off offset:3072
	global_load_dwordx2 v[36:37], v[2:3], off offset:3584
	global_load_dword v1, v10, s[10:11]
	global_load_dword v11, v10, s[4:5]
	s_mov_b32 s10, 0
	s_mov_b32 s11, 0x40f86a00
	s_mov_b32 s9, 0x3ee4f8b5
	v_mov_b32_e32 v38, 0x100
	v_mov_b32_e32 v39, 0xffffff80
	v_mov_b32_e32 v40, 0x260
	s_waitcnt vmcnt(17)
	v_add_f64 v[2:3], v[6:7], 0
	s_waitcnt vmcnt(16)
	v_add_f64 v[6:7], v[8:9], 0
	s_waitcnt vmcnt(15)
	v_add_f64 v[2:3], v[2:3], v[12:13]
	s_waitcnt vmcnt(14)
	v_add_f64 v[6:7], v[6:7], v[14:15]
	s_waitcnt vmcnt(13)
	v_add_f64 v[2:3], v[2:3], v[16:17]
	s_waitcnt vmcnt(12)
	v_add_f64 v[6:7], v[6:7], v[18:19]
	s_waitcnt vmcnt(11)
	v_add_f64 v[2:3], v[2:3], v[20:21]
	s_waitcnt vmcnt(10)
	v_add_f64 v[6:7], v[6:7], v[22:23]
	s_waitcnt vmcnt(9)
	v_add_f64 v[2:3], v[2:3], v[4:5]
	s_waitcnt vmcnt(8)
	v_add_f64 v[4:5], v[6:7], v[24:25]
	s_waitcnt vmcnt(7)
	v_add_f64 v[2:3], v[2:3], v[26:27]
	s_waitcnt vmcnt(6)
	v_add_f64 v[4:5], v[4:5], v[28:29]
	s_waitcnt vmcnt(5)
	v_add_f64 v[2:3], v[2:3], v[30:31]
	s_waitcnt vmcnt(4)
	v_add_f64 v[4:5], v[4:5], v[32:33]
	s_waitcnt vmcnt(3)
	v_add_f64 v[2:3], v[2:3], v[34:35]
	s_waitcnt vmcnt(2)
	v_add_f64 v[4:5], v[4:5], v[36:37]
	v_div_scale_f64 v[6:7], s[4:5], s[10:11], s[10:11], v[2:3]
	v_div_scale_f64 v[12:13], s[4:5], s[10:11], s[10:11], v[4:5]
	v_rcp_f64_e32 v[14:15], v[6:7]
	v_rcp_f64_e32 v[16:17], v[12:13]
	v_div_scale_f64 v[8:9], vcc, v[2:3], s[10:11], v[2:3]
	v_fma_f64 v[20:21], -v[6:7], v[14:15], 1.0
	v_fma_f64 v[22:23], -v[12:13], v[16:17], 1.0
	v_fmac_f64_e32 v[14:15], v[14:15], v[20:21]
	v_fmac_f64_e32 v[16:17], v[16:17], v[22:23]
	v_fma_f64 v[20:21], -v[6:7], v[14:15], 1.0
	v_fma_f64 v[22:23], -v[12:13], v[16:17], 1.0
	v_fmac_f64_e32 v[14:15], v[14:15], v[20:21]
	v_div_scale_f64 v[18:19], s[4:5], v[4:5], s[10:11], v[4:5]
	v_fmac_f64_e32 v[16:17], v[16:17], v[22:23]
	v_mul_f64 v[20:21], v[8:9], v[14:15]
	v_mul_f64 v[22:23], v[18:19], v[16:17]
	v_fma_f64 v[6:7], -v[6:7], v[20:21], v[8:9]
	v_fma_f64 v[8:9], -v[12:13], v[22:23], v[18:19]
	v_div_fmas_f64 v[6:7], v[6:7], v[14:15], v[20:21]
	s_mov_b64 vcc, s[4:5]
	v_div_fixup_f64 v[2:3], v[6:7], s[10:11], v[2:3]
	v_div_fmas_f64 v[6:7], v[8:9], v[16:17], v[22:23]
	v_div_fixup_f64 v[4:5], v[6:7], s[10:11], v[4:5]
	v_fma_f64 v[4:5], -v[2:3], v[2:3], v[4:5]
	v_cmp_ngt_f64_e32 vcc, 0, v[4:5]
	s_waitcnt vmcnt(1)
	v_cvt_f64_f32_e32 v[8:9], v1
	s_waitcnt vmcnt(0)
	v_cvt_f64_f32_e32 v[12:13], v11
	v_cndmask_b32_e32 v5, 0, v5, vcc
	v_cndmask_b32_e32 v4, 0, v4, vcc
	v_add_f64 v[4:5], v[4:5], s[8:9]
	v_cmp_gt_f64_e32 vcc, s[12:13], v[4:5]
	v_add_f64 v[2:3], v[2:3], 0
	s_nop 0
	v_cndmask_b32_e32 v6, 0, v38, vcc
	v_ldexp_f64 v[4:5], v[4:5], v6
	v_rsq_f64_e32 v[6:7], v[4:5]
	v_cndmask_b32_e32 v1, 0, v39, vcc
	v_cmp_class_f64_e32 vcc, v[4:5], v40
	v_mul_f64 v[14:15], v[4:5], v[6:7]
	v_mul_f64 v[6:7], v[6:7], 0.5
	v_fma_f64 v[16:17], -v[6:7], v[14:15], 0.5
	v_fmac_f64_e32 v[14:15], v[14:15], v[16:17]
	v_fmac_f64_e32 v[6:7], v[6:7], v[16:17]
	v_fma_f64 v[16:17], -v[14:15], v[14:15], v[4:5]
	v_fmac_f64_e32 v[14:15], v[16:17], v[6:7]
	v_fma_f64 v[16:17], -v[14:15], v[14:15], v[4:5]
	v_fmac_f64_e32 v[14:15], v[16:17], v[6:7]
	v_ldexp_f64 v[6:7], v[14:15], v1
	v_cndmask_b32_e32 v5, v7, v5, vcc
	v_cndmask_b32_e32 v4, v6, v4, vcc
	v_div_scale_f64 v[6:7], s[4:5], v[4:5], v[4:5], v[8:9]
	v_rcp_f64_e32 v[14:15], v[6:7]
	v_div_scale_f64 v[16:17], vcc, v[8:9], v[4:5], v[8:9]
	v_fma_f64 v[18:19], -v[6:7], v[14:15], 1.0
	v_fmac_f64_e32 v[14:15], v[14:15], v[18:19]
	v_fma_f64 v[18:19], -v[6:7], v[14:15], 1.0
	v_fmac_f64_e32 v[14:15], v[14:15], v[18:19]
	v_mul_f64 v[18:19], v[16:17], v[14:15]
	v_fma_f64 v[6:7], -v[6:7], v[18:19], v[16:17]
	v_div_fmas_f64 v[6:7], v[6:7], v[14:15], v[18:19]
	v_div_fixup_f64 v[4:5], v[6:7], v[4:5], v[8:9]
	v_fma_f64 v[2:3], -v[2:3], v[4:5], v[12:13]
	v_cvt_f32_f64_e32 v1, v[4:5]
	v_cvt_f32_f64_e32 v2, v[2:3]
	ds_write2st64_b32 v10, v1, v2 offset0:128 offset1:129

.Lu3_again:
	s_load_dword s3, s[0:1], 0x58
	v_lshrrev_b32_e32 v1, 6, v0
	s_waitcnt lgkmcnt(0)
	v_lshl_add_u32 v1, s2, 2, v1
	v_add_u32_e32 v1, s31, v1
	s_movk_i32 s2, 0xc35
	v_cmp_gt_i32_e32 vcc, s2, v1
	s_and_saveexec_b64 s[2:3], vcc
	s_cbranch_execz .LBB9_4
	s_load_dwordx4 s[4:7], s[0:1], 0x30
	s_load_dwordx2 s[2:3], s[0:1], 0x40
	s_load_dwordx4 s[8:11], s[0:1], 0x0
	v_and_b32_e32 v22, 31, v0
	v_lshlrev_b32_e32 v1, 5, v1
	v_or_b32_e32 v2, v1, v22
	v_ashrrev_i32_e32 v3, 31, v2
	v_lshlrev_b64 v[16:17], 7, v[2:3]
	v_and_b32_e32 v4, 32, v0
	s_waitcnt lgkmcnt(0)
	v_lshl_add_u64 v[2:3], s[10:11], 0, v[16:17]
	v_lshlrev_b32_e32 v28, 1, v4
	v_mov_b32_e32 v29, 0
	v_lshl_add_u64 v[18:19], v[2:3], 0, v[28:29]
	s_waitcnt vmcnt(0)
	v_mov_b32_e32 v2, v44
	v_mov_b32_e32 v3, v45
	v_mov_b32_e32 v4, v46
	v_mov_b32_e32 v5, v47
	v_mov_b32_e32 v6, v48
	v_mov_b32_e32 v7, v49
	v_mov_b32_e32 v8, v50
	v_mov_b32_e32 v9, v51
	v_mov_b32_e32 v12, v52
	v_mov_b32_e32 v13, v53
	v_mov_b32_e32 v14, v54
	v_mov_b32_e32 v15, v55
	v_mov_b32_e32 v24, v56
	v_mov_b32_e32 v25, v57
	v_mov_b32_e32 v26, v58
	v_mov_b32_e32 v27, v59
	v_lshl_add_u64 v[16:17], s[8:9], 0, v[16:17]
	v_lshl_add_u64 v[16:17], v[16:17], 0, v[28:29]
	v_and_b32_e32 v76, 0x80, v10
	v_and_b32_e32 v20, 63, v0
	v_lshrrev_b32_e32 v0, 3, v0
	v_and_or_b32 v0, v0, 4, v1
	v_ashrrev_i32_e32 v1, 31, v0
	s_waitcnt vmcnt(0)
	v_mov_b32_e32 v28, v60
	v_mov_b32_e32 v29, v61
	v_mov_b32_e32 v30, v62
	v_mov_b32_e32 v31, v63
	v_mov_b32_e32 v32, v64
	v_mov_b32_e32 v33, v65
	v_mov_b32_e32 v34, v66
	v_mov_b32_e32 v35, v67
	v_mov_b32_e32 v36, v68
	v_mov_b32_e32 v37, v69
	v_mov_b32_e32 v38, v70
	v_mov_b32_e32 v39, v71
	v_mov_b32_e32 v40, v72
	v_mov_b32_e32 v41, v73
	v_mov_b32_e32 v42, v74
	v_mov_b32_e32 v43, v75
	v_cvt_f32_f16_sdwa v17, v24 dst_sel:DWORD dst_unused:UNUSED_PAD src0_sel:WORD_1
	s_waitcnt vmcnt(0)
	v_lshlrev_b32_e32 v11, 16, v40
	v_and_b32_e32 v16, 0xffff0000, v40
	v_lshlrev_b32_e32 v21, 16, v41
	v_and_b32_e32 v23, 0xffff0000, v41
	v_lshlrev_b32_e32 v48, 16, v42
	v_and_b32_e32 v49, 0xffff0000, v42
	v_lshlrev_b32_e32 v50, 16, v43
	v_and_b32_e32 v51, 0xffff0000, v43
	v_lshlrev_b32_e32 v52, 16, v36
	v_and_b32_e32 v53, 0xffff0000, v36
	v_lshlrev_b32_e32 v54, 16, v37
	v_and_b32_e32 v55, 0xffff0000, v37
	v_lshlrev_b32_e32 v56, 16, v38
	v_and_b32_e32 v57, 0xffff0000, v38
	v_lshlrev_b32_e32 v58, 16, v39
	v_and_b32_e32 v59, 0xffff0000, v39
	v_lshlrev_b32_e32 v60, 16, v32
	v_and_b32_e32 v61, 0xffff0000, v32
	v_lshlrev_b32_e32 v62, 16, v33
	v_and_b32_e32 v63, 0xffff0000, v33
	v_lshlrev_b32_e32 v64, 16, v34
	v_and_b32_e32 v65, 0xffff0000, v34
	v_lshlrev_b32_e32 v66, 16, v35
	v_and_b32_e32 v67, 0xffff0000, v35
	v_lshlrev_b32_e32 v68, 16, v28
	v_and_b32_e32 v69, 0xffff0000, v28
	v_lshlrev_b32_e32 v70, 16, v29
	v_and_b32_e32 v71, 0xffff0000, v29
	v_lshlrev_b32_e32 v72, 16, v30
	v_and_b32_e32 v73, 0xffff0000, v30
	v_lshlrev_b32_e32 v74, 16, v31
	v_and_b32_e32 v75, 0xffff0000, v31
	ds_read_b128 v[28:31], v76 offset:32768
	ds_read_b128 v[32:35], v76 offset:32784
	ds_read_b128 v[36:39], v76 offset:32800
	ds_read_b128 v[40:43], v76 offset:32816
	ds_read_b128 v[44:47], v76 offset:33024
	s_waitcnt lgkmcnt(0)
	v_fma_f32 v10, v28, v11, v44
	v_fma_f32 v11, v29, v16, v45
	v_cvt_f32_f16_e32 v16, v24
	v_max_f32_e32 v10, 0, v10
	v_max_f32_e32 v11, 0, v11
	v_fmac_f32_e32 v47, v31, v23
	v_pk_add_f32 v[44:45], v[10:11], v[16:17]
	v_cvt_f32_f16_e32 v16, v25
	v_cvt_f32_f16_sdwa v17, v25 dst_sel:DWORD dst_unused:UNUSED_PAD src0_sel:WORD_1
	v_fma_f32 v10, v30, v21, v46
	ds_read_b128 v[28:31], v76 offset:33040
	v_max_f32_e32 v10, 0, v10
	v_max_f32_e32 v11, 0, v47
	v_pk_add_f32 v[46:47], v[10:11], v[16:17]
	v_cvt_f32_f16_e32 v16, v26
	v_cvt_f32_f16_sdwa v17, v26 dst_sel:DWORD dst_unused:UNUSED_PAD src0_sel:WORD_1
	s_waitcnt lgkmcnt(0)
	v_fma_f32 v10, v32, v48, v28
	v_fma_f32 v11, v33, v49, v29
	v_max_f32_e32 v10, 0, v10
	v_max_f32_e32 v11, 0, v11
	v_pk_add_f32 v[28:29], v[10:11], v[16:17]
	v_cvt_f32_f16_e32 v16, v27
	v_cvt_f32_f16_sdwa v17, v27 dst_sel:DWORD dst_unused:UNUSED_PAD src0_sel:WORD_1
	ds_read_b128 v[24:27], v76 offset:33056
	v_fma_f32 v10, v34, v50, v30
	v_fmac_f32_e32 v31, v35, v51
	v_max_f32_e32 v10, 0, v10
	v_max_f32_e32 v11, 0, v31
	v_pk_add_f32 v[30:31], v[10:11], v[16:17]
	v_cvt_f32_f16_e32 v16, v12
	v_cvt_f32_f16_sdwa v17, v12 dst_sel:DWORD dst_unused:UNUSED_PAD src0_sel:WORD_1
	s_waitcnt lgkmcnt(0)
	v_fma_f32 v10, v36, v52, v24
	v_fma_f32 v11, v37, v53, v25
	v_cvt_f32_f16_e32 v12, v13
	v_cvt_f32_f16_sdwa v13, v13 dst_sel:DWORD dst_unused:UNUSED_PAD src0_sel:WORD_1
	v_max_f32_e32 v10, 0, v10
	v_max_f32_e32 v11, 0, v11
	v_pk_add_f32 v[24:25], v[10:11], v[16:17]
	v_fma_f32 v10, v38, v54, v26
	v_fmac_f32_e32 v27, v39, v55
	v_max_f32_e32 v10, 0, v10
	v_max_f32_e32 v11, 0, v27
	v_pk_add_f32 v[26:27], v[10:11], v[12:13]
	ds_read_b128 v[10:13], v76 offset:33072
	v_cvt_f32_f16_e32 v16, v14
	v_cvt_f32_f16_sdwa v17, v14 dst_sel:DWORD dst_unused:UNUSED_PAD src0_sel:WORD_1
	v_lshlrev_b32_e32 v23, 4, v20
	s_waitcnt lgkmcnt(0)
	v_fma_f32 v10, v40, v56, v10
	v_fma_f32 v11, v41, v57, v11
	v_max_f32_e32 v10, 0, v10
	v_max_f32_e32 v11, 0, v11
	v_fmac_f32_e32 v13, v43, v59
	v_pk_add_f32 v[32:33], v[10:11], v[16:17]
	v_fma_f32 v10, v42, v58, v12
	v_max_f32_e32 v11, 0, v13
	v_cvt_f32_f16_e32 v12, v15
	v_cvt_f32_f16_sdwa v13, v15 dst_sel:DWORD dst_unused:UNUSED_PAD src0_sel:WORD_1
	v_max_f32_e32 v10, 0, v10
	v_pk_add_f32 v[34:35], v[10:11], v[12:13]
	ds_read_b128 v[10:13], v76 offset:32832
	ds_read_b128 v[14:17], v76 offset:33088
	s_waitcnt lgkmcnt(0)
	v_fma_f32 v10, v10, v60, v14
	v_fma_f32 v11, v11, v61, v15
	v_cvt_f32_f16_e32 v14, v6
	v_cvt_f32_f16_sdwa v15, v6 dst_sel:DWORD dst_unused:UNUSED_PAD src0_sel:WORD_1
	v_max_f32_e32 v10, 0, v10
	v_max_f32_e32 v11, 0, v11
	v_fma_f32 v6, v12, v62, v16
	v_pk_add_f32 v[36:37], v[10:11], v[14:15]
	v_max_f32_e32 v10, 0, v6
	v_cvt_f32_f16_e32 v6, v7
	v_cvt_f32_f16_sdwa v7, v7 dst_sel:DWORD dst_unused:UNUSED_PAD src0_sel:WORD_1
	v_fmac_f32_e32 v17, v13, v63
	v_max_f32_e32 v11, 0, v17
	v_pk_add_f32 v[38:39], v[10:11], v[6:7]
	ds_read_b128 v[10:13], v76 offset:32848
	ds_read_b128 v[14:17], v76 offset:33104
	s_waitcnt lgkmcnt(0)
	v_fma_f32 v6, v10, v64, v14
	v_fma_f32 v7, v11, v65, v15
	v_cvt_f32_f16_e32 v10, v8
	v_cvt_f32_f16_sdwa v11, v8 dst_sel:DWORD dst_unused:UNUSED_PAD src0_sel:WORD_1
	v_cvt_f32_f16_e32 v8, v9
	v_cvt_f32_f16_sdwa v9, v9 dst_sel:DWORD dst_unused:UNUSED_PAD src0_sel:WORD_1
	v_max_f32_e32 v6, 0, v6
	v_max_f32_e32 v7, 0, v7
	v_pk_add_f32 v[40:41], v[6:7], v[10:11]
	v_fma_f32 v6, v12, v66, v16
	v_fmac_f32_e32 v17, v13, v67
	v_max_f32_e32 v6, 0, v6
	v_max_f32_e32 v7, 0, v17
	v_pk_add_f32 v[42:43], v[6:7], v[8:9]
	ds_read_b128 v[6:9], v76 offset:32864
	ds_read_b128 v[10:13], v76 offset:33120
	v_cvt_pk_f16_f32 v14, v44, v45
	v_cvt_pk_f16_f32 v15, v46, v47
	v_cvt_pk_f16_f32 v16, v28, v29
	v_cvt_pk_f16_f32 v17, v30, v31
	s_waitcnt lgkmcnt(0)
	v_fma_f32 v6, v6, v68, v10
	v_fma_f32 v7, v7, v69, v11
	v_cvt_f32_f16_e32 v10, v2
	v_cvt_f32_f16_sdwa v11, v2 dst_sel:DWORD dst_unused:UNUSED_PAD src0_sel:WORD_1
	v_max_f32_e32 v6, 0, v6
	v_max_f32_e32 v7, 0, v7
	v_fma_f32 v2, v8, v70, v12
	v_pk_add_f32 v[48:49], v[6:7], v[10:11]
	v_max_f32_e32 v6, 0, v2
	v_cvt_f32_f16_e32 v2, v3
	v_cvt_f32_f16_sdwa v3, v3 dst_sel:DWORD dst_unused:UNUSED_PAD src0_sel:WORD_1
	v_fmac_f32_e32 v13, v9, v71
	v_max_f32_e32 v7, 0, v13
	v_pk_add_f32 v[50:51], v[6:7], v[2:3]
	ds_read_b128 v[6:9], v76 offset:32880
	ds_read_b128 v[10:13], v76 offset:33136
	global_store_dwordx4 v[18:19], v[14:17], off
	s_waitcnt lgkmcnt(0)
	v_fma_f32 v2, v6, v72, v10
	v_fma_f32 v3, v7, v73, v11
	v_cvt_f32_f16_e32 v6, v4
	v_cvt_f32_f16_sdwa v7, v4 dst_sel:DWORD dst_unused:UNUSED_PAD src0_sel:WORD_1
	v_cvt_f32_f16_e32 v4, v5
	v_cvt_f32_f16_sdwa v5, v5 dst_sel:DWORD dst_unused:UNUSED_PAD src0_sel:WORD_1
	v_max_f32_e32 v2, 0, v2
	v_max_f32_e32 v3, 0, v3
	v_pk_add_f32 v[52:53], v[2:3], v[6:7]
	v_fma_f32 v2, v8, v74, v12
	v_fmac_f32_e32 v13, v9, v75
	v_max_f32_e32 v2, 0, v2
	v_max_f32_e32 v3, 0, v13
	v_pk_add_f32 v[54:55], v[2:3], v[4:5]
	v_cvt_pk_f16_f32 v10, v24, v25
	v_cvt_pk_f16_f32 v11, v26, v27
	v_cvt_pk_f16_f32 v12, v32, v33
	v_cvt_pk_f16_f32 v13, v34, v35
	v_cvt_pk_f16_f32 v6, v36, v37
	v_cvt_pk_f16_f32 v7, v38, v39
	v_cvt_pk_f16_f32 v8, v40, v41
	v_cvt_pk_f16_f32 v9, v42, v43
	v_cvt_pk_f16_f32 v2, v48, v49
	v_cvt_pk_f16_f32 v3, v50, v51
	v_cvt_pk_f16_f32 v4, v52, v53
	v_cvt_pk_f16_f32 v5, v54, v55
	global_store_dwordx4 v[18:19], v[10:13], off offset:16
	global_store_dwordx4 v[18:19], v[6:9], off offset:32
	global_store_dwordx4 v[18:19], v[2:5], off offset:48
	ds_read_b128 v[18:21], v23
	ds_read_b128 v[24:27], v23 offset:8192
	ds_read_b128 v[28:31], v23 offset:4096
	ds_read_b128 v[32:35], v23 offset:12288
	v_accvgpr_mov_b32 a16, a0
	v_accvgpr_mov_b32 a17, a0
	v_accvgpr_mov_b32 a18, a0
	v_accvgpr_mov_b32 a19, a0
	v_accvgpr_mov_b32 a20, a0
	v_accvgpr_mov_b32 a21, a0
	v_accvgpr_mov_b32 a22, a0
	v_accvgpr_mov_b32 a23, a0
	v_accvgpr_mov_b32 a24, a0
	v_accvgpr_mov_b32 a25, a0
	v_accvgpr_mov_b32 a26, a0
	v_accvgpr_mov_b32 a27, a0
	v_accvgpr_mov_b32 a28, a0
	v_accvgpr_mov_b32 a29, a0
	v_accvgpr_mov_b32 a30, a0
	v_accvgpr_mov_b32 a31, a0
	v_accvgpr_mov_b32 a0, a1
	v_accvgpr_mov_b32 a2, a1
	v_accvgpr_mov_b32 a3, a1
	v_accvgpr_mov_b32 a4, a1
	v_accvgpr_mov_b32 a5, a1
	v_accvgpr_mov_b32 a6, a1
	v_accvgpr_mov_b32 a7, a1
	v_accvgpr_mov_b32 a8, a1
	v_accvgpr_mov_b32 a9, a1
	v_accvgpr_mov_b32 a10, a1
	v_accvgpr_mov_b32 a11, a1
	v_accvgpr_mov_b32 a12, a1
	v_accvgpr_mov_b32 a13, a1
	v_accvgpr_mov_b32 a14, a1
	v_accvgpr_mov_b32 a15, a1
	s_waitcnt lgkmcnt(3)
	v_mfma_f32_32x32x16_f16 a[16:31], v[14:17], v[18:21], a[16:31]
	s_waitcnt lgkmcnt(1)
	v_mfma_f32_32x32x16_f16 a[0:15], v[14:17], v[28:31], a[0:15]
	v_mfma_f32_32x32x16_f16 a[16:31], v[14:17], v[24:27], a[16:31]
	s_waitcnt lgkmcnt(0)
	v_mfma_f32_32x32x16_f16 a[0:15], v[14:17], v[32:35], a[0:15]
	ds_read_b128 v[18:21], v23 offset:1024
	ds_read_b128 v[24:27], v23 offset:9216
	ds_read_b128 v[28:31], v23 offset:5120
	ds_read_b128 v[32:35], v23 offset:13312
	s_waitcnt lgkmcnt(3)
	v_mfma_f32_32x32x16_f16 a[16:31], v[10:13], v[18:21], a[16:31]
	s_waitcnt lgkmcnt(1)
	v_mfma_f32_32x32x16_f16 a[0:15], v[10:13], v[28:31], a[0:15]
	v_mfma_f32_32x32x16_f16 a[16:31], v[10:13], v[24:27], a[16:31]
	s_waitcnt lgkmcnt(0)
	v_mfma_f32_32x32x16_f16 a[0:15], v[10:13], v[32:35], a[0:15]
	ds_read_b128 v[18:21], v23 offset:2048
	ds_read_b128 v[24:27], v23 offset:10240
	ds_read_b128 v[28:31], v23 offset:6144
	ds_read_b128 v[32:35], v23 offset:14336
	s_waitcnt lgkmcnt(3)
	v_mfma_f32_32x32x16_f16 a[16:31], v[6:9], v[18:21], a[16:31]
	s_waitcnt lgkmcnt(1)
	v_mfma_f32_32x32x16_f16 a[0:15], v[6:9], v[28:31], a[0:15]
	v_mfma_f32_32x32x16_f16 a[16:31], v[6:9], v[24:27], a[16:31]
	s_waitcnt lgkmcnt(0)
	v_mfma_f32_32x32x16_f16 a[0:15], v[6:9], v[32:35], a[0:15]
	ds_read_b128 v[18:21], v23 offset:3072
	ds_read_b128 v[24:27], v23 offset:11264
	ds_read_b128 v[28:31], v23 offset:7168
	ds_read_b128 v[32:35], v23 offset:15360
	s_waitcnt lgkmcnt(3)
	v_mfma_f32_32x32x16_f16 a[16:31], v[2:5], v[18:21], a[16:31]
	s_waitcnt lgkmcnt(1)
	v_mfma_f32_32x32x16_f16 a[0:15], v[2:5], v[28:31], a[0:15]
	v_mfma_f32_32x32x16_f16 a[16:31], v[2:5], v[24:27], a[16:31]
	s_waitcnt lgkmcnt(0)
	v_mfma_f32_32x32x16_f16 a[0:15], v[2:5], v[32:35], a[0:15]
	ds_read_b128 v[18:21], v23 offset:16384
	ds_read_b128 v[24:27], v23 offset:24576
	ds_read_b128 v[28:31], v23 offset:20480
	ds_read_b128 v[32:35], v23 offset:28672
	s_waitcnt lgkmcnt(3)
	v_mfma_f32_32x32x16_f16 a[32:47], v[14:17], v[18:21], 0
	s_waitcnt lgkmcnt(1)
	v_mfma_f32_32x32x16_f16 a[48:63], v[14:17], v[28:31], 0
	v_mfma_f32_32x32x16_f16 a[32:47], v[14:17], v[24:27], a[32:47]
	s_waitcnt lgkmcnt(0)
	v_mfma_f32_32x32x16_f16 a[48:63], v[14:17], v[32:35], a[48:63]
	ds_read_b128 v[14:17], v23 offset:17408
	ds_read_b128 v[18:21], v23 offset:25600
	ds_read_b128 v[24:27], v23 offset:21504
	ds_read_b128 v[28:31], v23 offset:29696
	s_waitcnt lgkmcnt(3)
	v_mfma_f32_32x32x16_f16 a[32:47], v[10:13], v[14:17], a[32:47]
	s_waitcnt lgkmcnt(1)
	v_mfma_f32_32x32x16_f16 a[48:63], v[10:13], v[24:27], a[48:63]
	v_mfma_f32_32x32x16_f16 a[32:47], v[10:13], v[18:21], a[32:47]
	s_waitcnt lgkmcnt(0)
	v_mfma_f32_32x32x16_f16 a[48:63], v[10:13], v[28:31], a[48:63]
	ds_read_b128 v[10:13], v23 offset:18432
	ds_read_b128 v[14:17], v23 offset:26624
	ds_read_b128 v[18:21], v23 offset:22528
	ds_read_b128 v[24:27], v23 offset:30720
	s_waitcnt lgkmcnt(3)
	v_mfma_f32_32x32x16_f16 a[32:47], v[6:9], v[10:13], a[32:47]
	s_waitcnt lgkmcnt(1)
	v_mfma_f32_32x32x16_f16 a[48:63], v[6:9], v[18:21], a[48:63]
	v_mfma_f32_32x32x16_f16 a[32:47], v[6:9], v[14:17], a[32:47]
	s_waitcnt lgkmcnt(0)
	v_mfma_f32_32x32x16_f16 a[48:63], v[6:9], v[24:27], a[48:63]
	ds_read_b128 v[10:13], v23 offset:19456
	ds_read_b128 v[6:9], v23 offset:27648
	ds_read_b128 v[18:21], v23 offset:23552
	ds_read_b128 v[14:17], v23 offset:31744
	s_waitcnt lgkmcnt(3)
	v_mfma_f32_32x32x16_f16 a[32:47], v[2:5], v[10:13], a[32:47]
	s_waitcnt lgkmcnt(1)
	v_mfma_f32_32x32x16_f16 a[48:63], v[2:5], v[18:21], a[48:63]
	v_mfma_f32_32x32x16_f16 a[32:47], v[2:5], v[6:9], a[32:47]
	v_lshlrev_b32_e32 v7, 2, v22
	s_waitcnt lgkmcnt(0)
	v_mfma_f32_32x32x16_f16 a[48:63], v[2:5], v[14:17], a[48:63]
	v_accvgpr_read_b32 v2, a0
	v_accvgpr_read_b32 v3, a16
	v_cvt_pk_bf16_f32 v6, v3, v2
	v_lshlrev_b64 v[2:3], 7, v[0:1]
	v_or_b32_e32 v2, v2, v7
	v_lshl_add_u64 v[4:5], s[6:7], 0, v[2:3]
	global_store_dword v[4:5], v6, off
	s_nop 1
	v_accvgpr_read_b32 v4, a32
	v_lshl_add_u64 v[2:3], s[2:3], 0, v[2:3]
	s_nop 0
	v_accvgpr_read_b32 v1, a48
	v_cvt_pk_bf16_f32 v1, v4, v1
	global_store_dword v[2:3], v1, off
	v_or_b32_e32 v2, 1, v0
	v_ashrrev_i32_e32 v3, 31, v2
	v_lshlrev_b64 v[2:3], 7, v[2:3]
	v_accvgpr_read_b32 v1, a1
	v_accvgpr_read_b32 v4, a17
	v_or_b32_e32 v2, v2, v7
	v_cvt_pk_bf16_f32 v1, v4, v1
	v_lshl_add_u64 v[4:5], s[6:7], 0, v[2:3]
	global_store_dword v[4:5], v1, off
	v_accvgpr_read_b32 v1, a49
	v_accvgpr_read_b32 v4, a33
	v_cvt_pk_bf16_f32 v1, v4, v1
	v_lshl_add_u64 v[2:3], s[2:3], 0, v[2:3]
	global_store_dword v[2:3], v1, off
	v_or_b32_e32 v2, 2, v0
	v_ashrrev_i32_e32 v3, 31, v2
	v_lshlrev_b64 v[2:3], 7, v[2:3]
	v_accvgpr_read_b32 v1, a2
	v_accvgpr_read_b32 v4, a18
	v_or_b32_e32 v2, v2, v7
	v_cvt_pk_bf16_f32 v1, v4, v1
	v_lshl_add_u64 v[4:5], s[6:7], 0, v[2:3]
	global_store_dword v[4:5], v1, off
	v_accvgpr_read_b32 v1, a50
	v_accvgpr_read_b32 v4, a34
	v_cvt_pk_bf16_f32 v1, v4, v1
	v_lshl_add_u64 v[2:3], s[2:3], 0, v[2:3]
	global_store_dword v[2:3], v1, off
	v_or_b32_e32 v2, 3, v0
	v_ashrrev_i32_e32 v3, 31, v2
	v_lshlrev_b64 v[2:3], 7, v[2:3]
	v_accvgpr_read_b32 v1, a3
	v_accvgpr_read_b32 v4, a19
	v_or_b32_e32 v2, v2, v7
	v_cvt_pk_bf16_f32 v1, v4, v1
	v_lshl_add_u64 v[4:5], s[6:7], 0, v[2:3]
	global_store_dword v[4:5], v1, off
	v_accvgpr_read_b32 v1, a51
	v_accvgpr_read_b32 v4, a35
	v_cvt_pk_bf16_f32 v1, v4, v1
	v_lshl_add_u64 v[2:3], s[2:3], 0, v[2:3]
	global_store_dword v[2:3], v1, off
	v_or_b32_e32 v2, 8, v0
	v_ashrrev_i32_e32 v3, 31, v2
	v_lshlrev_b64 v[2:3], 7, v[2:3]
	v_accvgpr_read_b32 v1, a4
	v_accvgpr_read_b32 v4, a20
	v_or_b32_e32 v2, v2, v7
	v_cvt_pk_bf16_f32 v1, v4, v1
	v_lshl_add_u64 v[4:5], s[6:7], 0, v[2:3]
	global_store_dword v[4:5], v1, off
	v_accvgpr_read_b32 v1, a52
	v_accvgpr_read_b32 v4, a36
	v_cvt_pk_bf16_f32 v1, v4, v1
	v_lshl_add_u64 v[2:3], s[2:3], 0, v[2:3]
	global_store_dword v[2:3], v1, off
	v_or_b32_e32 v2, 9, v0
	v_ashrrev_i32_e32 v3, 31, v2
	v_lshlrev_b64 v[2:3], 7, v[2:3]
	v_accvgpr_read_b32 v1, a5
	v_accvgpr_read_b32 v4, a21
	v_or_b32_e32 v2, v2, v7
	v_cvt_pk_bf16_f32 v1, v4, v1
	v_lshl_add_u64 v[4:5], s[6:7], 0, v[2:3]
	global_store_dword v[4:5], v1, off
	v_accvgpr_read_b32 v1, a53
	v_accvgpr_read_b32 v4, a37
	v_cvt_pk_bf16_f32 v1, v4, v1
	v_lshl_add_u64 v[2:3], s[2:3], 0, v[2:3]
	global_store_dword v[2:3], v1, off
	v_or_b32_e32 v2, 10, v0
	v_ashrrev_i32_e32 v3, 31, v2
	v_lshlrev_b64 v[2:3], 7, v[2:3]
	v_accvgpr_read_b32 v1, a6
	v_accvgpr_read_b32 v4, a22
	v_or_b32_e32 v2, v2, v7
	v_cvt_pk_bf16_f32 v1, v4, v1
	v_lshl_add_u64 v[4:5], s[6:7], 0, v[2:3]
	global_store_dword v[4:5], v1, off
	v_accvgpr_read_b32 v1, a54
	v_accvgpr_read_b32 v4, a38
	v_cvt_pk_bf16_f32 v1, v4, v1
	v_lshl_add_u64 v[2:3], s[2:3], 0, v[2:3]
	global_store_dword v[2:3], v1, off
	v_or_b32_e32 v2, 11, v0
	v_ashrrev_i32_e32 v3, 31, v2
	v_lshlrev_b64 v[2:3], 7, v[2:3]
	v_accvgpr_read_b32 v1, a7
	v_accvgpr_read_b32 v4, a23
	v_or_b32_e32 v2, v2, v7
	v_cvt_pk_bf16_f32 v1, v4, v1
	v_lshl_add_u64 v[4:5], s[6:7], 0, v[2:3]
	global_store_dword v[4:5], v1, off
	v_accvgpr_read_b32 v1, a55
	v_accvgpr_read_b32 v4, a39
	v_cvt_pk_bf16_f32 v1, v4, v1
	v_lshl_add_u64 v[2:3], s[2:3], 0, v[2:3]
	global_store_dword v[2:3], v1, off
	v_or_b32_e32 v2, 16, v0
	v_ashrrev_i32_e32 v3, 31, v2
	v_lshlrev_b64 v[2:3], 7, v[2:3]
	v_accvgpr_read_b32 v1, a8
	v_accvgpr_read_b32 v4, a24
	v_or_b32_e32 v2, v2, v7
	v_cvt_pk_bf16_f32 v1, v4, v1
	v_lshl_add_u64 v[4:5], s[6:7], 0, v[2:3]
	global_store_dword v[4:5], v1, off
	v_accvgpr_read_b32 v1, a56
	v_accvgpr_read_b32 v4, a40
	v_cvt_pk_bf16_f32 v1, v4, v1
	v_lshl_add_u64 v[2:3], s[2:3], 0, v[2:3]
	global_store_dword v[2:3], v1, off
	v_or_b32_e32 v2, 17, v0
	v_ashrrev_i32_e32 v3, 31, v2
	v_lshlrev_b64 v[2:3], 7, v[2:3]
	v_accvgpr_read_b32 v1, a9
	v_accvgpr_read_b32 v4, a25
	v_or_b32_e32 v2, v2, v7
	v_cvt_pk_bf16_f32 v1, v4, v1
	v_lshl_add_u64 v[4:5], s[6:7], 0, v[2:3]
	global_store_dword v[4:5], v1, off
	v_accvgpr_read_b32 v1, a57
	v_accvgpr_read_b32 v4, a41
	v_cvt_pk_bf16_f32 v1, v4, v1
	v_lshl_add_u64 v[2:3], s[2:3], 0, v[2:3]
	global_store_dword v[2:3], v1, off
	v_or_b32_e32 v2, 18, v0
	v_ashrrev_i32_e32 v3, 31, v2
	v_lshlrev_b64 v[2:3], 7, v[2:3]
	v_accvgpr_read_b32 v1, a10
	v_accvgpr_read_b32 v4, a26
	v_or_b32_e32 v2, v2, v7
	v_cvt_pk_bf16_f32 v1, v4, v1
	v_lshl_add_u64 v[4:5], s[6:7], 0, v[2:3]
	global_store_dword v[4:5], v1, off
	v_accvgpr_read_b32 v1, a58
	v_accvgpr_read_b32 v4, a42
	v_cvt_pk_bf16_f32 v1, v4, v1
	v_lshl_add_u64 v[2:3], s[2:3], 0, v[2:3]
	global_store_dword v[2:3], v1, off
	v_or_b32_e32 v2, 19, v0
	v_ashrrev_i32_e32 v3, 31, v2
	v_lshlrev_b64 v[2:3], 7, v[2:3]
	v_accvgpr_read_b32 v1, a11
	v_accvgpr_read_b32 v4, a27
	v_or_b32_e32 v2, v2, v7
	v_cvt_pk_bf16_f32 v1, v4, v1
	v_lshl_add_u64 v[4:5], s[6:7], 0, v[2:3]
	global_store_dword v[4:5], v1, off
	v_accvgpr_read_b32 v1, a59
	v_accvgpr_read_b32 v4, a43
	v_cvt_pk_bf16_f32 v1, v4, v1
	v_lshl_add_u64 v[2:3], s[2:3], 0, v[2:3]
	global_store_dword v[2:3], v1, off
	v_or_b32_e32 v2, 24, v0
	v_ashrrev_i32_e32 v3, 31, v2
	v_lshlrev_b64 v[2:3], 7, v[2:3]
	v_accvgpr_read_b32 v1, a12
	v_accvgpr_read_b32 v4, a28
	v_or_b32_e32 v2, v2, v7
	v_cvt_pk_bf16_f32 v1, v4, v1
	v_lshl_add_u64 v[4:5], s[6:7], 0, v[2:3]
	global_store_dword v[4:5], v1, off
	v_accvgpr_read_b32 v1, a60
	v_accvgpr_read_b32 v4, a44
	v_cvt_pk_bf16_f32 v1, v4, v1
	v_lshl_add_u64 v[2:3], s[2:3], 0, v[2:3]
	global_store_dword v[2:3], v1, off
	v_or_b32_e32 v2, 25, v0
	v_ashrrev_i32_e32 v3, 31, v2
	v_lshlrev_b64 v[2:3], 7, v[2:3]
	v_accvgpr_read_b32 v1, a13
	v_accvgpr_read_b32 v4, a29
	v_or_b32_e32 v2, v2, v7
	v_cvt_pk_bf16_f32 v1, v4, v1
	v_lshl_add_u64 v[4:5], s[6:7], 0, v[2:3]
	global_store_dword v[4:5], v1, off
	v_accvgpr_read_b32 v1, a61
	v_accvgpr_read_b32 v4, a45
	v_cvt_pk_bf16_f32 v1, v4, v1
	v_lshl_add_u64 v[2:3], s[2:3], 0, v[2:3]
	global_store_dword v[2:3], v1, off
	v_or_b32_e32 v2, 26, v0
	v_ashrrev_i32_e32 v3, 31, v2
	v_lshlrev_b64 v[2:3], 7, v[2:3]
	v_accvgpr_read_b32 v1, a14
	v_accvgpr_read_b32 v4, a30
	v_or_b32_e32 v2, v2, v7
	v_cvt_pk_bf16_f32 v1, v4, v1
	v_lshl_add_u64 v[4:5], s[6:7], 0, v[2:3]
	global_store_dword v[4:5], v1, off
	v_accvgpr_read_b32 v1, a62
	v_accvgpr_read_b32 v4, a46
	v_cvt_pk_bf16_f32 v1, v4, v1
	v_lshl_add_u64 v[2:3], s[2:3], 0, v[2:3]
	v_or_b32_e32 v0, 27, v0
	global_store_dword v[2:3], v1, off
	v_ashrrev_i32_e32 v1, 31, v0
	v_lshlrev_b64 v[0:1], 7, v[0:1]
	v_accvgpr_read_b32 v2, a15
	v_accvgpr_read_b32 v3, a31
	v_or_b32_e32 v0, v0, v7
	v_cvt_pk_bf16_f32 v4, v3, v2
	v_lshl_add_u64 v[2:3], s[6:7], 0, v[0:1]
	global_store_dword v[2:3], v4, off
	v_accvgpr_read_b32 v2, a63
	v_accvgpr_read_b32 v3, a47
	v_cvt_pk_bf16_f32 v2, v3, v2
	v_lshl_add_u64 v[0:1], s[2:3], 0, v[0:1]
	global_store_dword v[0:1], v2, off
	s_cmp_lg_u32 s31, 0
	s_cbranch_scc1 .LBB9_4
	s_mov_b64 exec, -1
	v_lshrrev_b32_e32 v78, 6, v77
	s_lshl_b32 s33, s30, 2
	v_readfirstlane_b32 s32, v78
	s_add_i32 s32, s32, s33
	s_cmp_ge_u32 s32, 53
	s_cbranch_scc1 .LBB9_4
	s_movk_i32 s31, 0xc00
	s_mov_b32 s2, s30
	v_mov_b32_e32 v0, v77
	v_mov_b32_e32 v10, v79
	s_add_i32 s32, s32, 0xc00
	s_lshl_b32 s32, s32, 5
	v_and_b32_e32 v78, 31, v0
	v_or_b32_e32 v78, s32, v78
	v_lshlrev_b32_e32 v78, 7, v78
	v_and_b32_e32 v1, 32, v0
	v_lshl_add_u32 v78, v1, 1, v78
	global_load_dwordx4 v[44:47], v78, s[22:23] offset:48
	global_load_dwordx4 v[48:51], v78, s[22:23] offset:32
	global_load_dwordx4 v[52:55], v78, s[22:23] offset:16
	global_load_dwordx4 v[56:59], v78, s[22:23]
	global_load_dwordx4 v[60:63], v78, s[20:21] offset:48
	global_load_dwordx4 v[64:67], v78, s[20:21] offset:32
	global_load_dwordx4 v[68:71], v78, s[20:21] offset:16
	global_load_dwordx4 v[72:75], v78, s[20:21]
	v_and_b32_e32 v1, 31, v0
	v_lshlrev_b32_e32 v1, 3, v1
	global_load_dwordx2 a[0:1], v1, s[24:25]
	s_waitcnt vmcnt(0)
	s_branch .Lu3_again
